# moved the 16 sunk fp8 MFMAs of SP1 back between their barrier pair in the three fp8 GEMM loops (P7 x2, P15)
# speedup vs baseline: 1.0143x; 1.0143x over previous
; #define PG8_STAGE(bufoff, gbase, voff) do { _Pragma("unroll") for (int _i = 0; _i < 2; ++_i) { unsigned vo_ = (voff)[_i]; asm volatile("" : "+v"(vo_));   \
;         __builtin_amdgcn_global_load_lds((const unsigned*)((const char*)(gbase) + vo_), (LAS unsigned*)(lds + (bufoff) + ldsw + _i * 8192), 16, 0, 0); } } while (0)
; #define PG8_LDA(dst, b, h) do { _Pragma("unroll") for (int m = 0; m < 4; ++m) _Pragma("unroll") for (int k = 0; k < 2; ++k) dst[m][k] = *(const LAS bf16x8*)(lds + PG8_SA(b, h) + aoff + m * 2048 + k * 1024); } while (0)
; #define PG8_LDB(dst, b, h) do { _Pragma("unroll") for (int n = 0; n < 2; ++n) _Pragma("unroll") for (int k = 0; k < 2; ++k) dst[n][k] = *(const LAS bf16x8*)(lds + PG8_SB(b, h) + boff + n * 2048 + k * 1024); } while (0)
; #define PG8_WAIT_V(n) asm volatile("s_waitcnt vmcnt(" #n ")" ::: "memory")
; #define PG8_WAIT_L(n) asm volatile("s_waitcnt lgkmcnt(" #n ")" ::: "memory")
; #define PG8_BAR __builtin_amdgcn_s_barrier()
; #define PG8_SCHED __builtin_amdgcn_sched_barrier(0)
; #define PG8_AOFFS(dst, un) do { _Pragma("unroll") for (int _h = 0; _h < 2; ++_h) _Pragma("unroll") for (int _i = 0; _i < 2; ++_i) dst[_h][_i] = S.Aoff(un, _h * HALF + Rr[_i]) + (unsigned)Cc[_i] * 2u; } while (0)
;     ...
;             PG8_LDB(B0, 0, 0); PG8_LDB(B1, 0, 1); PG8_SCHED; PG8_LDA(At, 0, 0); PG8_STAGE(PG8_SA(1, 1), a1, va[1]);
;             PG8_WAIT_V(8); PG8_WAIT_L(0); PG8_BAR; PG8_MMA(0, 0, At, B0); PG8_MMA(0, 1, At, B1); PG8_BAR; PG8_SCHED;
;             if (last && has_next) { PG8_AOFFS(va, nxt); }
;             PG8_LDA(At, 0, 1); PG8_STAGE(PG8_SB(0, 0), b2, voffB); PG8_STAGE(PG8_SB(0, 1), b2 + hstepB, voffB); PG8_STAGE(PG8_SA(0, 0), a2, va[0]);
;             PG8_WAIT_V(8); PG8_WAIT_L(0); PG8_BAR; PG8_MMA(1, 0, At, B0); PG8_MMA(1, 1, At, B1); PG8_BAR; PG8_SCHED;
;             PG8_LDB(B0, 1, 0); PG8_LDB(B1, 1, 1); PG8_SCHED; PG8_LDA(At, 1, 0); PG8_STAGE(PG8_SA(0, 1), a2, va[1]);
;             PG8_WAIT_V(8); PG8_WAIT_L(0); PG8_BAR; PG8_MMA(0, 0, At, B0); PG8_MMA(0, 1, At, B1); PG8_BAR; PG8_SCHED;
;             PG8_LDA(At, 1, 1); PG8_STAGE(PG8_SB(1, 0), b3, voffB); PG8_STAGE(PG8_SB(1, 1), b3 + hstepB, voffB); PG8_STAGE(PG8_SA(1, 0), a3, va[0]);
;             PG8_WAIT_V(8); PG8_WAIT_L(0); PG8_BAR; PG8_MMA(1, 0, At, B0); PG8_MMA(1, 1, At, B1); PG8_BAR; PG8_SCHED;
.LBB0_1531:
	ds_read_b128 v[18:21], v228
	ds_read_b128 v[22:25], v228 offset:1024
	ds_read_b128 v[26:29], v228 offset:2048
	ds_read_b128 v[30:33], v228 offset:3072
	ds_read_b128 v[2:5], v229
	ds_read_b128 v[6:9], v229 offset:1024
	ds_read_b128 v[10:13], v229 offset:2048
	ds_read_b128 v[14:17], v229 offset:3072
	s_cmp_eq_u32 s67, 40
	s_cselect_b64 s[42:43], -1, 0
	v_mov_b32_e32 v194, v224
	s_add_u32 s30, s18, s40
	s_mov_b32 m0, s61
	ds_read_b128 v[58:61], v230
	ds_read_b128 v[62:65], v230 offset:1024
	ds_read_b128 v[50:53], v230 offset:2048
	ds_read_b128 v[54:57], v230 offset:3072
	ds_read_b128 v[42:45], v230 offset:4096
	ds_read_b128 v[46:49], v230 offset:5120
	ds_read_b128 v[34:37], v230 offset:6144
	ds_read_b128 v[38:41], v230 offset:7168
	s_addc_u32 s31, s19, s41
	global_load_lds_dwordx4 v194, s[30:31]
	v_mov_b32_e32 v194, v225
	s_add_i32 m0, s45, 0xe000
	s_nop 0
	global_load_lds_dwordx4 v194, s[30:31]
	s_waitcnt vmcnt(8)
	s_waitcnt lgkmcnt(0)
	s_barrier
	s_setprio 1
	s_waitcnt lgkmcnt(0)
	v_mfma_scale_f32_16x16x128_f8f6f4 v[190:193], v[18:25], v[58:65], v[190:193], v231, v231 op_sel_hi:[0,0,0]
	v_mfma_scale_f32_16x16x128_f8f6f4 v[186:189], v[26:33], v[58:65], v[186:189], v231, v231 op_sel_hi:[0,0,0]
	v_mfma_scale_f32_16x16x128_f8f6f4 v[174:177], v[18:25], v[50:57], v[174:177], v231, v231 op_sel_hi:[0,0,0]
	v_mfma_scale_f32_16x16x128_f8f6f4 v[170:173], v[26:33], v[50:57], v[170:173], v231, v231 op_sel_hi:[0,0,0]
	v_mfma_scale_f32_16x16x128_f8f6f4 v[158:161], v[18:25], v[42:49], v[158:161], v231, v231 op_sel_hi:[0,0,0]
	v_mfma_scale_f32_16x16x128_f8f6f4 v[154:157], v[26:33], v[42:49], v[154:157], v231, v231 op_sel_hi:[0,0,0]
	v_mfma_scale_f32_16x16x128_f8f6f4 v[142:145], v[18:25], v[34:41], v[142:145], v231, v231 op_sel_hi:[0,0,0]
	v_mfma_scale_f32_16x16x128_f8f6f4 v[138:141], v[26:33], v[34:41], v[138:141], v231, v231 op_sel_hi:[0,0,0]
	s_setprio 0
	s_setprio 1
	v_mfma_scale_f32_16x16x128_f8f6f4 v[182:185], v[2:9], v[58:65], v[182:185], v231, v231 op_sel_hi:[0,0,0]
	v_mfma_scale_f32_16x16x128_f8f6f4 v[178:181], v[10:17], v[58:65], v[178:181], v231, v231 op_sel_hi:[0,0,0]
	v_mfma_scale_f32_16x16x128_f8f6f4 v[166:169], v[2:9], v[50:57], v[166:169], v231, v231 op_sel_hi:[0,0,0]
	v_mfma_scale_f32_16x16x128_f8f6f4 v[162:165], v[10:17], v[50:57], v[162:165], v231, v231 op_sel_hi:[0,0,0]
	v_mfma_scale_f32_16x16x128_f8f6f4 v[150:153], v[2:9], v[42:49], v[150:153], v231, v231 op_sel_hi:[0,0,0]
	v_mfma_scale_f32_16x16x128_f8f6f4 v[146:149], v[10:17], v[42:49], v[146:149], v231, v231 op_sel_hi:[0,0,0]
	v_mfma_scale_f32_16x16x128_f8f6f4 v[134:137], v[2:9], v[34:41], v[134:137], v231, v231 op_sel_hi:[0,0,0]
	v_mfma_scale_f32_16x16x128_f8f6f4 v[130:133], v[10:17], v[34:41], v[130:133], v231, v231 op_sel_hi:[0,0,0]
	s_setprio 0
	s_barrier
	s_and_b64 s[30:31], s[28:29], s[42:43]
	s_andn2_b64 vcc, exec, s[30:31]
	s_cbranch_vccnz .LBB0_1533
	v_mov_b32_e32 v225, v235
	v_mov_b32_e32 v224, v234
	v_mov_b32_e32 v223, v233
	v_mov_b32_e32 v222, v232
.LBB0_1533:
	s_add_u32 s30, s40, 0x100
	s_addc_u32 s31, s41, 0
	s_and_b64 s[34:35], s[42:43], exec
	s_cselect_b32 s34, 0, s30
	s_cselect_b32 s35, 0, s31
	s_add_u32 s34, s4, s34
	s_addc_u32 s35, s5, s35
	s_add_u32 s68, s14, s40
	s_addc_u32 s69, s27, s41
	s_and_b64 s[40:41], s[42:43], exec
	v_mov_b32_e32 v194, v215
	s_waitcnt lgkmcnt(0)
	s_cselect_b32 s41, s25, s69
	s_cselect_b32 s40, s24, s68
	s_mov_b32 m0, s46
	s_add_u32 s42, s40, 0xb0000
	s_addc_u32 s43, s41, 0
	ds_read_b128 v[58:61], v230 offset:16384
	ds_read_b128 v[62:65], v230 offset:17408
	ds_read_b128 v[50:53], v230 offset:18432
	ds_read_b128 v[54:57], v230 offset:19456
	ds_read_b128 v[42:45], v230 offset:20480
	ds_read_b128 v[46:49], v230 offset:21504
	ds_read_b128 v[34:37], v230 offset:22528
	ds_read_b128 v[38:41], v230 offset:23552
	s_nop 0
	global_load_lds_dwordx4 v194, s[40:41]
	v_mov_b32_e32 v194, v217
	s_mov_b32 m0, s47
	s_nop 0
	global_load_lds_dwordx4 v194, s[40:41]
	v_mov_b32_e32 v194, v215
	s_mov_b32 m0, s48
	s_nop 0
	global_load_lds_dwordx4 v194, s[42:43]
	v_mov_b32_e32 v194, v217
	s_mov_b32 m0, s49
	s_nop 0
	global_load_lds_dwordx4 v194, s[42:43]
	v_mov_b32_e32 v194, v222
	s_mov_b32 m0, s45
	s_nop 0
	global_load_lds_dwordx4 v194, s[34:35]
	v_mov_b32_e32 v194, v223
	s_mov_b32 m0, s50
	s_nop 0
	global_load_lds_dwordx4 v194, s[34:35]
	s_waitcnt vmcnt(8)
	s_waitcnt lgkmcnt(0)
	s_barrier
	s_setprio 1
	s_waitcnt lgkmcnt(0)
	v_mfma_scale_f32_16x16x128_f8f6f4 v[126:129], v[18:25], v[58:65], v[126:129], v231, v231 op_sel_hi:[0,0,0]
	v_mfma_scale_f32_16x16x128_f8f6f4 v[122:125], v[26:33], v[58:65], v[122:125], v231, v231 op_sel_hi:[0,0,0]
	v_mfma_scale_f32_16x16x128_f8f6f4 v[114:117], v[18:25], v[50:57], v[114:117], v231, v231 op_sel_hi:[0,0,0]
	v_mfma_scale_f32_16x16x128_f8f6f4 v[106:109], v[26:33], v[50:57], v[106:109], v231, v231 op_sel_hi:[0,0,0]
	v_mfma_scale_f32_16x16x128_f8f6f4 v[98:101], v[18:25], v[42:49], v[98:101], v231, v231 op_sel_hi:[0,0,0]
	v_mfma_scale_f32_16x16x128_f8f6f4 v[90:93], v[26:33], v[42:49], v[90:93], v231, v231 op_sel_hi:[0,0,0]
	v_mfma_scale_f32_16x16x128_f8f6f4 v[82:85], v[18:25], v[34:41], v[82:85], v231, v231 op_sel_hi:[0,0,0]
	v_mfma_scale_f32_16x16x128_f8f6f4 v[74:77], v[26:33], v[34:41], v[74:77], v231, v231 op_sel_hi:[0,0,0]
	s_setprio 0
	s_setprio 1
	v_mfma_scale_f32_16x16x128_f8f6f4 v[118:121], v[2:9], v[58:65], v[118:121], v231, v231 op_sel_hi:[0,0,0]
	v_mfma_scale_f32_16x16x128_f8f6f4 v[110:113], v[10:17], v[58:65], v[110:113], v231, v231 op_sel_hi:[0,0,0]
	v_mfma_scale_f32_16x16x128_f8f6f4 v[102:105], v[2:9], v[50:57], v[102:105], v231, v231 op_sel_hi:[0,0,0]
	v_mfma_scale_f32_16x16x128_f8f6f4 v[94:97], v[10:17], v[50:57], v[94:97], v231, v231 op_sel_hi:[0,0,0]
	v_mfma_scale_f32_16x16x128_f8f6f4 v[86:89], v[2:9], v[42:49], v[86:89], v231, v231 op_sel_hi:[0,0,0]
	v_mfma_scale_f32_16x16x128_f8f6f4 v[78:81], v[10:17], v[42:49], v[78:81], v231, v231 op_sel_hi:[0,0,0]
	v_mfma_scale_f32_16x16x128_f8f6f4 v[70:73], v[2:9], v[34:41], v[70:73], v231, v231 op_sel_hi:[0,0,0]
	v_mfma_scale_f32_16x16x128_f8f6f4 v[66:69], v[10:17], v[34:41], v[66:69], v231, v231 op_sel_hi:[0,0,0]
	s_setprio 0
	s_barrier
; #define PG8_STAGE(bufoff, gbase, voff) do { _Pragma("unroll") for (int _i = 0; _i < 2; ++_i) { unsigned vo_ = (voff)[_i]; asm volatile("" : "+v"(vo_));   \
;         __builtin_amdgcn_global_load_lds((const unsigned*)((const char*)(gbase) + vo_), (LAS unsigned*)(lds + (bufoff) + ldsw + _i * 8192), 16, 0, 0); } } while (0)
; #define PG8_LDA(dst, b, h) do { _Pragma("unroll") for (int m = 0; m < 4; ++m) _Pragma("unroll") for (int k = 0; k < 2; ++k) dst[m][k] = *(const LAS bf16x8*)(lds + PG8_SA(b, h) + aoff + m * 2048 + k * 1024); } while (0)
; #define PG8_LDB(dst, b, h) do { _Pragma("unroll") for (int n = 0; n < 2; ++n) _Pragma("unroll") for (int k = 0; k < 2; ++k) dst[n][k] = *(const LAS bf16x8*)(lds + PG8_SB(b, h) + boff + n * 2048 + k * 1024); } while (0)
; #define PG8_WAIT_V(n) asm volatile("s_waitcnt vmcnt(" #n ")" ::: "memory")
; #define PG8_WAIT_L(n) asm volatile("s_waitcnt lgkmcnt(" #n ")" ::: "memory")
; #define PG8_BAR __builtin_amdgcn_s_barrier()
; #define PG8_SCHED __builtin_amdgcn_sched_barrier(0)
; #define PG8_AOFFS(dst, un) do { _Pragma("unroll") for (int _h = 0; _h < 2; ++_h) _Pragma("unroll") for (int _i = 0; _i < 2; ++_i) dst[_h][_i] = S.Aoff(un, _h * HALF + Rr[_i]) + (unsigned)Cc[_i] * 2u; } while (0)
;     ...
;             PG8_LDB(B0, 0, 0); PG8_LDB(B1, 0, 1); PG8_SCHED; PG8_LDA(At, 0, 0); PG8_STAGE(PG8_SA(1, 1), a1, va[1]);
;             PG8_WAIT_V(8); PG8_WAIT_L(0); PG8_BAR; PG8_MMA(0, 0, At, B0); PG8_MMA(0, 1, At, B1); PG8_BAR; PG8_SCHED;
;             if (last && has_next) { PG8_AOFFS(va, nxt); }
;             PG8_LDA(At, 0, 1); PG8_STAGE(PG8_SB(0, 0), b2, voffB); PG8_STAGE(PG8_SB(0, 1), b2 + hstepB, voffB); PG8_STAGE(PG8_SA(0, 0), a2, va[0]);
;             PG8_WAIT_V(8); PG8_WAIT_L(0); PG8_BAR; PG8_MMA(1, 0, At, B0); PG8_MMA(1, 1, At, B1); PG8_BAR; PG8_SCHED;
;             PG8_LDB(B0, 1, 0); PG8_LDB(B1, 1, 1); PG8_SCHED; PG8_LDA(At, 1, 0); PG8_STAGE(PG8_SA(0, 1), a2, va[1]);
;             PG8_WAIT_V(8); PG8_WAIT_L(0); PG8_BAR; PG8_MMA(0, 0, At, B0); PG8_MMA(0, 1, At, B1); PG8_BAR; PG8_SCHED;
;             PG8_LDA(At, 1, 1); PG8_STAGE(PG8_SB(1, 0), b3, voffB); PG8_STAGE(PG8_SB(1, 1), b3 + hstepB, voffB); PG8_STAGE(PG8_SA(1, 0), a3, va[0]);
;             PG8_WAIT_V(8); PG8_WAIT_L(0); PG8_BAR; PG8_MMA(1, 0, At, B0); PG8_MMA(1, 1, At, B1); PG8_BAR; PG8_SCHED;
	s_add_i32 s42, 0, 0x18000
	s_add_i32 s43, 0, 0x1c000
	v_add_u32_e32 v14, s42, v226
	v_add_u32_e32 v30, s43, v226
	ds_read_b128 v[2:5], v14
	ds_read_b128 v[6:9], v14 offset:1024
	ds_read_b128 v[10:13], v14 offset:2048
	ds_read_b128 v[14:17], v14 offset:3072
	ds_read_b128 v[18:21], v30
	ds_read_b128 v[22:25], v30 offset:1024
	ds_read_b128 v[26:29], v30 offset:2048
	ds_read_b128 v[30:33], v30 offset:3072
	v_mov_b32_e32 v194, v224
	s_mov_b32 m0, s51
	ds_read_b128 v[34:37], v230 offset:32768
	ds_read_b128 v[38:41], v230 offset:33792
	ds_read_b128 v[42:45], v230 offset:34816
	ds_read_b128 v[46:49], v230 offset:35840
	ds_read_b128 v[50:53], v230 offset:36864
	ds_read_b128 v[54:57], v230 offset:37888
	ds_read_b128 v[58:61], v230 offset:38912
	ds_read_b128 v[62:65], v230 offset:39936
	s_nop 0
	global_load_lds_dwordx4 v194, s[34:35]
	v_mov_b32_e32 v194, v225
	s_mov_b32 m0, s52
	s_nop 0
	global_load_lds_dwordx4 v194, s[34:35]
	s_waitcnt vmcnt(8)
	s_waitcnt lgkmcnt(0)
	s_barrier
	s_setprio 1
	s_waitcnt lgkmcnt(0)
	v_mfma_scale_f32_16x16x128_f8f6f4 v[190:193], v[2:9], v[34:41], v[190:193], v231, v231 op_sel_hi:[0,0,0]
	v_mfma_scale_f32_16x16x128_f8f6f4 v[186:189], v[10:17], v[34:41], v[186:189], v231, v231 op_sel_hi:[0,0,0]
	v_mfma_scale_f32_16x16x128_f8f6f4 v[174:177], v[2:9], v[42:49], v[174:177], v231, v231 op_sel_hi:[0,0,0]
	v_mfma_scale_f32_16x16x128_f8f6f4 v[170:173], v[10:17], v[42:49], v[170:173], v231, v231 op_sel_hi:[0,0,0]
	v_mfma_scale_f32_16x16x128_f8f6f4 v[158:161], v[2:9], v[50:57], v[158:161], v231, v231 op_sel_hi:[0,0,0]
	v_mfma_scale_f32_16x16x128_f8f6f4 v[154:157], v[10:17], v[50:57], v[154:157], v231, v231 op_sel_hi:[0,0,0]
	v_mfma_scale_f32_16x16x128_f8f6f4 v[142:145], v[2:9], v[58:65], v[142:145], v231, v231 op_sel_hi:[0,0,0]
	v_mfma_scale_f32_16x16x128_f8f6f4 v[138:141], v[10:17], v[58:65], v[138:141], v231, v231 op_sel_hi:[0,0,0]
	s_setprio 0
	s_setprio 1
	v_mfma_scale_f32_16x16x128_f8f6f4 v[182:185], v[18:25], v[34:41], v[182:185], v231, v231 op_sel_hi:[0,0,0]
	v_mfma_scale_f32_16x16x128_f8f6f4 v[178:181], v[26:33], v[34:41], v[178:181], v231, v231 op_sel_hi:[0,0,0]
	v_mfma_scale_f32_16x16x128_f8f6f4 v[166:169], v[18:25], v[42:49], v[166:169], v231, v231 op_sel_hi:[0,0,0]
	v_mfma_scale_f32_16x16x128_f8f6f4 v[162:165], v[26:33], v[42:49], v[162:165], v231, v231 op_sel_hi:[0,0,0]
	v_mfma_scale_f32_16x16x128_f8f6f4 v[150:153], v[18:25], v[50:57], v[150:153], v231, v231 op_sel_hi:[0,0,0]
	v_mfma_scale_f32_16x16x128_f8f6f4 v[146:149], v[26:33], v[50:57], v[146:149], v231, v231 op_sel_hi:[0,0,0]
	v_mfma_scale_f32_16x16x128_f8f6f4 v[134:137], v[18:25], v[58:65], v[134:137], v231, v231 op_sel_hi:[0,0,0]
	v_mfma_scale_f32_16x16x128_f8f6f4 v[130:133], v[26:33], v[58:65], v[130:133], v231, v231 op_sel_hi:[0,0,0]
	s_setprio 0
	s_barrier
	v_mov_b32_e32 v194, v215
	ds_read_b128 v[34:37], v230 offset:49152
	ds_read_b128 v[38:41], v230 offset:50176
	ds_read_b128 v[42:45], v230 offset:51200
	ds_read_b128 v[46:49], v230 offset:52224
	ds_read_b128 v[50:53], v230 offset:53248
	ds_read_b128 v[54:57], v230 offset:54272
	ds_read_b128 v[58:61], v230 offset:55296
	ds_read_b128 v[62:65], v230 offset:56320
	s_add_i32 s42, s42, s38
	v_lshl_add_u64 v[236:237], s[40:41], 0, v[194:195]
	v_lshl_add_u64 v[236:237], v[236:237], 0, s[16:17]
	s_mov_b32 m0, s42
	v_mov_b32_e32 v194, v217
	global_load_lds_dwordx4 v[236:237], off
	s_add_i32 m0, s42, 0x2000
	s_nop 0
	v_lshl_add_u64 v[236:237], s[40:41], 0, v[194:195]
	s_add_u32 s40, s40, 0xb0080
	v_lshl_add_u64 v[236:237], v[236:237], 0, s[16:17]
	s_addc_u32 s41, s41, 0
	v_mov_b32_e32 v194, v215
	s_add_i32 s42, s43, s38
	global_load_lds_dwordx4 v[236:237], off
	s_mov_b32 m0, s42
	s_nop 0
	global_load_lds_dwordx4 v194, s[40:41]
	v_mov_b32_e32 v194, v217
	s_add_i32 m0, s42, 0x2000
	s_nop 0
	global_load_lds_dwordx4 v194, s[40:41]
	v_mov_b32_e32 v194, v222
	s_mov_b32 m0, s59
	v_lshl_add_u64 v[236:237], s[34:35], 0, v[194:195]
	v_lshl_add_u64 v[236:237], v[236:237], 0, s[16:17]
	v_mov_b32_e32 v194, v223
	global_load_lds_dwordx4 v[236:237], off
	s_mov_b32 m0, s60
	v_lshl_add_u64 v[236:237], s[34:35], 0, v[194:195]
	v_lshl_add_u64 v[236:237], v[236:237], 0, s[16:17]
	global_load_lds_dwordx4 v[236:237], off
	s_waitcnt vmcnt(8)
	s_waitcnt lgkmcnt(0)
	s_barrier
	s_setprio 1
	s_waitcnt lgkmcnt(0)
	v_mfma_scale_f32_16x16x128_f8f6f4 v[126:129], v[2:9], v[34:41], v[126:129], v231, v231 op_sel_hi:[0,0,0]
	v_mfma_scale_f32_16x16x128_f8f6f4 v[122:125], v[10:17], v[34:41], v[122:125], v231, v231 op_sel_hi:[0,0,0]
	v_mfma_scale_f32_16x16x128_f8f6f4 v[114:117], v[2:9], v[42:49], v[114:117], v231, v231 op_sel_hi:[0,0,0]
	v_mfma_scale_f32_16x16x128_f8f6f4 v[106:109], v[10:17], v[42:49], v[106:109], v231, v231 op_sel_hi:[0,0,0]
	v_mfma_scale_f32_16x16x128_f8f6f4 v[98:101], v[2:9], v[50:57], v[98:101], v231, v231 op_sel_hi:[0,0,0]
	v_mfma_scale_f32_16x16x128_f8f6f4 v[90:93], v[10:17], v[50:57], v[90:93], v231, v231 op_sel_hi:[0,0,0]
	v_mfma_scale_f32_16x16x128_f8f6f4 v[82:85], v[2:9], v[58:65], v[82:85], v231, v231 op_sel_hi:[0,0,0]
	v_mfma_scale_f32_16x16x128_f8f6f4 v[74:77], v[10:17], v[58:65], v[74:77], v231, v231 op_sel_hi:[0,0,0]
	s_setprio 0
	s_setprio 1
	v_mfma_scale_f32_16x16x128_f8f6f4 v[118:121], v[18:25], v[34:41], v[118:121], v231, v231 op_sel_hi:[0,0,0]
	v_mfma_scale_f32_16x16x128_f8f6f4 v[110:113], v[26:33], v[34:41], v[110:113], v231, v231 op_sel_hi:[0,0,0]
	v_mfma_scale_f32_16x16x128_f8f6f4 v[102:105], v[18:25], v[42:49], v[102:105], v231, v231 op_sel_hi:[0,0,0]
	v_mfma_scale_f32_16x16x128_f8f6f4 v[94:97], v[26:33], v[42:49], v[94:97], v231, v231 op_sel_hi:[0,0,0]
	v_mfma_scale_f32_16x16x128_f8f6f4 v[86:89], v[18:25], v[50:57], v[86:89], v231, v231 op_sel_hi:[0,0,0]
	v_mfma_scale_f32_16x16x128_f8f6f4 v[78:81], v[26:33], v[50:57], v[78:81], v231, v231 op_sel_hi:[0,0,0]
	v_mfma_scale_f32_16x16x128_f8f6f4 v[70:73], v[18:25], v[58:65], v[70:73], v231, v231 op_sel_hi:[0,0,0]
	v_mfma_scale_f32_16x16x128_f8f6f4 v[66:69], v[26:33], v[58:65], v[66:69], v231, v231 op_sel_hi:[0,0,0]
	s_setprio 0
	s_barrier
	s_add_i32 s67, s67, 2
	s_cmp_gt_u32 s67, 41
	s_cbranch_scc1 .LBB0_1535
	s_mov_b64 s[40:41], s[30:31]
	s_branch .LBB0_1531

; #define PG8_STAGE(bufoff, gbase, voff) do { _Pragma("unroll") for (int _i = 0; _i < 2; ++_i) { unsigned vo_ = (voff)[_i]; asm volatile("" : "+v"(vo_));   \
;         __builtin_amdgcn_global_load_lds((const unsigned*)((const char*)(gbase) + vo_), (LAS unsigned*)(lds + (bufoff) + ldsw + _i * 8192), 16, 0, 0); } } while (0)
; #define PG8_LDA(dst, b, h) do { _Pragma("unroll") for (int m = 0; m < 4; ++m) _Pragma("unroll") for (int k = 0; k < 2; ++k) dst[m][k] = *(const LAS bf16x8*)(lds + PG8_SA(b, h) + aoff + m * 2048 + k * 1024); } while (0)
; #define PG8_LDB(dst, b, h) do { _Pragma("unroll") for (int n = 0; n < 2; ++n) _Pragma("unroll") for (int k = 0; k < 2; ++k) dst[n][k] = *(const LAS bf16x8*)(lds + PG8_SB(b, h) + boff + n * 2048 + k * 1024); } while (0)
; #define PG8_WAIT_V(n) asm volatile("s_waitcnt vmcnt(" #n ")" ::: "memory")
; #define PG8_WAIT_L(n) asm volatile("s_waitcnt lgkmcnt(" #n ")" ::: "memory")
; #define PG8_BAR __builtin_amdgcn_s_barrier()
; #define PG8_SCHED __builtin_amdgcn_sched_barrier(0)
; #define PG8_AOFFS(dst, un) do { _Pragma("unroll") for (int _h = 0; _h < 2; ++_h) _Pragma("unroll") for (int _i = 0; _i < 2; ++_i) dst[_h][_i] = S.Aoff(un, _h * HALF + Rr[_i]) + (unsigned)Cc[_i] * 2u; } while (0)
;     ...
;             PG8_LDB(B0, 0, 0); PG8_LDB(B1, 0, 1); PG8_SCHED; PG8_LDA(At, 0, 0); PG8_STAGE(PG8_SA(1, 1), a1, va[1]);
;             PG8_WAIT_V(8); PG8_WAIT_L(0); PG8_BAR; PG8_MMA(0, 0, At, B0); PG8_MMA(0, 1, At, B1); PG8_BAR; PG8_SCHED;
;             if (last && has_next) { PG8_AOFFS(va, nxt); }
;             PG8_LDA(At, 0, 1); PG8_STAGE(PG8_SB(0, 0), b2, voffB); PG8_STAGE(PG8_SB(0, 1), b2 + hstepB, voffB); PG8_STAGE(PG8_SA(0, 0), a2, va[0]);
;             PG8_WAIT_V(8); PG8_WAIT_L(0); PG8_BAR; PG8_MMA(1, 0, At, B0); PG8_MMA(1, 1, At, B1); PG8_BAR; PG8_SCHED;
;             PG8_LDB(B0, 1, 0); PG8_LDB(B1, 1, 1); PG8_SCHED; PG8_LDA(At, 1, 0); PG8_STAGE(PG8_SA(0, 1), a2, va[1]);
;             PG8_WAIT_V(8); PG8_WAIT_L(0); PG8_BAR; PG8_MMA(0, 0, At, B0); PG8_MMA(0, 1, At, B1); PG8_BAR; PG8_SCHED;
;             PG8_LDA(At, 1, 1); PG8_STAGE(PG8_SB(1, 0), b3, voffB); PG8_STAGE(PG8_SB(1, 1), b3 + hstepB, voffB); PG8_STAGE(PG8_SA(1, 0), a3, va[0]);
;             PG8_WAIT_V(8); PG8_WAIT_L(0); PG8_BAR; PG8_MMA(1, 0, At, B0); PG8_MMA(1, 1, At, B1); PG8_BAR; PG8_SCHED;
.LBB0_1564:
	ds_read_b128 v[18:21], v220
	ds_read_b128 v[22:25], v220 offset:1024
	ds_read_b128 v[26:29], v220 offset:2048
	ds_read_b128 v[30:33], v220 offset:3072
	ds_read_b128 v[2:5], v221
	ds_read_b128 v[6:9], v221 offset:1024
	ds_read_b128 v[10:13], v221 offset:2048
	ds_read_b128 v[14:17], v221 offset:3072
	s_cmp_eq_u32 s27, s71
	s_cselect_b64 s[48:49], -1, 0
	s_add_i32 m0, s51, 0xc000
	v_mov_b32_e32 v194, v224
	s_add_u32 s42, s16, s46
	ds_read_b128 v[58:61], v226
	ds_read_b128 v[62:65], v226 offset:1024
	ds_read_b128 v[50:53], v226 offset:2048
	ds_read_b128 v[54:57], v226 offset:3072
	ds_read_b128 v[42:45], v226 offset:4096
	ds_read_b128 v[46:49], v226 offset:5120
	ds_read_b128 v[34:37], v226 offset:6144
	ds_read_b128 v[38:41], v226 offset:7168
	s_addc_u32 s43, s17, s47
	global_load_lds_dwordx4 v194, s[42:43]
	v_mov_b32_e32 v194, v225
	s_add_i32 m0, s51, 0xe000
	s_nop 0
	global_load_lds_dwordx4 v194, s[42:43]
	s_waitcnt vmcnt(8)
	s_waitcnt lgkmcnt(0)
	s_barrier
	s_setprio 1
	s_waitcnt lgkmcnt(0)
	v_mfma_scale_f32_16x16x128_f8f6f4 v[178:181], v[18:25], v[58:65], v[178:181], v227, v227 op_sel_hi:[0,0,0]
	v_mfma_scale_f32_16x16x128_f8f6f4 v[182:185], v[26:33], v[58:65], v[182:185], v227, v227 op_sel_hi:[0,0,0]
	v_mfma_scale_f32_16x16x128_f8f6f4 v[174:177], v[18:25], v[50:57], v[174:177], v227, v227 op_sel_hi:[0,0,0]
	v_mfma_scale_f32_16x16x128_f8f6f4 v[166:169], v[26:33], v[50:57], v[166:169], v227, v227 op_sel_hi:[0,0,0]
	v_mfma_scale_f32_16x16x128_f8f6f4 v[162:165], v[18:25], v[42:49], v[162:165], v227, v227 op_sel_hi:[0,0,0]
	v_mfma_scale_f32_16x16x128_f8f6f4 v[154:157], v[26:33], v[42:49], v[154:157], v227, v227 op_sel_hi:[0,0,0]
	v_mfma_scale_f32_16x16x128_f8f6f4 v[150:153], v[18:25], v[34:41], v[150:153], v227, v227 op_sel_hi:[0,0,0]
	v_mfma_scale_f32_16x16x128_f8f6f4 v[142:145], v[26:33], v[34:41], v[142:145], v227, v227 op_sel_hi:[0,0,0]
	s_setprio 0
	s_setprio 1
	v_mfma_scale_f32_16x16x128_f8f6f4 v[186:189], v[2:9], v[58:65], v[186:189], v227, v227 op_sel_hi:[0,0,0]
	v_mfma_scale_f32_16x16x128_f8f6f4 v[190:193], v[10:17], v[58:65], v[190:193], v227, v227 op_sel_hi:[0,0,0]
	v_mfma_scale_f32_16x16x128_f8f6f4 v[170:173], v[2:9], v[50:57], v[170:173], v227, v227 op_sel_hi:[0,0,0]
	v_mfma_scale_f32_16x16x128_f8f6f4 v[158:161], v[10:17], v[50:57], v[158:161], v227, v227 op_sel_hi:[0,0,0]
	v_mfma_scale_f32_16x16x128_f8f6f4 v[146:149], v[2:9], v[42:49], v[146:149], v227, v227 op_sel_hi:[0,0,0]
	v_mfma_scale_f32_16x16x128_f8f6f4 v[138:141], v[10:17], v[42:49], v[138:141], v227, v227 op_sel_hi:[0,0,0]
	v_mfma_scale_f32_16x16x128_f8f6f4 v[134:137], v[2:9], v[34:41], v[134:137], v227, v227 op_sel_hi:[0,0,0]
	v_mfma_scale_f32_16x16x128_f8f6f4 v[130:133], v[10:17], v[34:41], v[130:133], v227, v227 op_sel_hi:[0,0,0]
	s_setprio 0
	s_barrier
	s_and_b64 s[42:43], s[40:41], s[48:49]
	s_andn2_b64 vcc, exec, s[42:43]
	s_cbranch_vccnz .LBB0_1566
	v_mov_b32_e32 v225, v231
	v_mov_b32_e32 v224, v230
	v_mov_b32_e32 v223, v229
	v_mov_b32_e32 v222, v228
.LBB0_1566:
	s_add_i32 s71, s71, 2
	s_add_u32 s42, s46, 0x100
	s_addc_u32 s43, s47, 0
	s_and_b64 s[44:45], s[48:49], exec
	s_cselect_b32 s44, 0, s42
	s_cselect_b32 s45, 0, s43
	s_add_u32 s44, s4, s44
	s_addc_u32 s45, s5, s45
	s_add_u32 s72, s69, s46
	s_addc_u32 s73, s70, s47
	s_and_b64 s[46:47], s[48:49], exec
	v_mov_b32_e32 v194, v215
	s_waitcnt lgkmcnt(0)
	s_cselect_b32 s47, s29, s73
	s_cselect_b32 s46, s28, s72
	s_mov_b32 m0, s52
	s_add_u32 s48, s46, 0xb0000
	s_addc_u32 s49, s47, 0
	ds_read_b128 v[58:61], v226 offset:16384
	ds_read_b128 v[62:65], v226 offset:17408
	ds_read_b128 v[50:53], v226 offset:18432
	ds_read_b128 v[54:57], v226 offset:19456
	ds_read_b128 v[42:45], v226 offset:20480
	ds_read_b128 v[46:49], v226 offset:21504
	ds_read_b128 v[34:37], v226 offset:22528
	ds_read_b128 v[38:41], v226 offset:23552
	s_nop 0
	global_load_lds_dwordx4 v194, s[46:47]
	v_mov_b32_e32 v194, v217
	s_mov_b32 m0, s53
	s_nop 0
	global_load_lds_dwordx4 v194, s[46:47]
	v_mov_b32_e32 v194, v215
	s_mov_b32 m0, s54
	s_nop 0
	global_load_lds_dwordx4 v194, s[48:49]
	v_mov_b32_e32 v194, v217
	s_mov_b32 m0, s55
	s_nop 0
	global_load_lds_dwordx4 v194, s[48:49]
	v_mov_b32_e32 v194, v222
	s_mov_b32 m0, s51
	s_nop 0
	global_load_lds_dwordx4 v194, s[44:45]
	v_mov_b32_e32 v194, v223
	s_mov_b32 m0, s56
	s_nop 0
	global_load_lds_dwordx4 v194, s[44:45]
	s_waitcnt vmcnt(8)
	s_waitcnt lgkmcnt(0)
	s_barrier
	s_setprio 1
	s_waitcnt lgkmcnt(0)
	v_mfma_scale_f32_16x16x128_f8f6f4 v[126:129], v[18:25], v[58:65], v[126:129], v227, v227 op_sel_hi:[0,0,0]
	v_mfma_scale_f32_16x16x128_f8f6f4 v[122:125], v[26:33], v[58:65], v[122:125], v227, v227 op_sel_hi:[0,0,0]
	v_mfma_scale_f32_16x16x128_f8f6f4 v[114:117], v[18:25], v[50:57], v[114:117], v227, v227 op_sel_hi:[0,0,0]
	v_mfma_scale_f32_16x16x128_f8f6f4 v[110:113], v[26:33], v[50:57], v[110:113], v227, v227 op_sel_hi:[0,0,0]
	v_mfma_scale_f32_16x16x128_f8f6f4 v[102:105], v[18:25], v[42:49], v[102:105], v227, v227 op_sel_hi:[0,0,0]
	v_mfma_scale_f32_16x16x128_f8f6f4 v[94:97], v[26:33], v[42:49], v[94:97], v227, v227 op_sel_hi:[0,0,0]
	v_mfma_scale_f32_16x16x128_f8f6f4 v[86:89], v[18:25], v[34:41], v[86:89], v227, v227 op_sel_hi:[0,0,0]
	v_mfma_scale_f32_16x16x128_f8f6f4 v[78:81], v[26:33], v[34:41], v[78:81], v227, v227 op_sel_hi:[0,0,0]
	s_setprio 0
	s_setprio 1
	v_mfma_scale_f32_16x16x128_f8f6f4 v[118:121], v[2:9], v[58:65], v[118:121], v227, v227 op_sel_hi:[0,0,0]
	v_mfma_scale_f32_16x16x128_f8f6f4 v[106:109], v[10:17], v[58:65], v[106:109], v227, v227 op_sel_hi:[0,0,0]
	v_mfma_scale_f32_16x16x128_f8f6f4 v[98:101], v[2:9], v[50:57], v[98:101], v227, v227 op_sel_hi:[0,0,0]
	v_mfma_scale_f32_16x16x128_f8f6f4 v[90:93], v[10:17], v[50:57], v[90:93], v227, v227 op_sel_hi:[0,0,0]
	v_mfma_scale_f32_16x16x128_f8f6f4 v[82:85], v[2:9], v[42:49], v[82:85], v227, v227 op_sel_hi:[0,0,0]
	v_mfma_scale_f32_16x16x128_f8f6f4 v[74:77], v[10:17], v[42:49], v[74:77], v227, v227 op_sel_hi:[0,0,0]
	v_mfma_scale_f32_16x16x128_f8f6f4 v[70:73], v[2:9], v[34:41], v[70:73], v227, v227 op_sel_hi:[0,0,0]
	v_mfma_scale_f32_16x16x128_f8f6f4 v[66:69], v[10:17], v[34:41], v[66:69], v227, v227 op_sel_hi:[0,0,0]
	s_setprio 0
	s_barrier
; #define PG8_STAGE(bufoff, gbase, voff) do { _Pragma("unroll") for (int _i = 0; _i < 2; ++_i) { unsigned vo_ = (voff)[_i]; asm volatile("" : "+v"(vo_));   \
;         __builtin_amdgcn_global_load_lds((const unsigned*)((const char*)(gbase) + vo_), (LAS unsigned*)(lds + (bufoff) + ldsw + _i * 8192), 16, 0, 0); } } while (0)
; #define PG8_LDA(dst, b, h) do { _Pragma("unroll") for (int m = 0; m < 4; ++m) _Pragma("unroll") for (int k = 0; k < 2; ++k) dst[m][k] = *(const LAS bf16x8*)(lds + PG8_SA(b, h) + aoff + m * 2048 + k * 1024); } while (0)
; #define PG8_LDB(dst, b, h) do { _Pragma("unroll") for (int n = 0; n < 2; ++n) _Pragma("unroll") for (int k = 0; k < 2; ++k) dst[n][k] = *(const LAS bf16x8*)(lds + PG8_SB(b, h) + boff + n * 2048 + k * 1024); } while (0)
; #define PG8_WAIT_V(n) asm volatile("s_waitcnt vmcnt(" #n ")" ::: "memory")
; #define PG8_WAIT_L(n) asm volatile("s_waitcnt lgkmcnt(" #n ")" ::: "memory")
; #define PG8_BAR __builtin_amdgcn_s_barrier()
; #define PG8_SCHED __builtin_amdgcn_sched_barrier(0)
; #define PG8_AOFFS(dst, un) do { _Pragma("unroll") for (int _h = 0; _h < 2; ++_h) _Pragma("unroll") for (int _i = 0; _i < 2; ++_i) dst[_h][_i] = S.Aoff(un, _h * HALF + Rr[_i]) + (unsigned)Cc[_i] * 2u; } while (0)
;     ...
;             PG8_LDB(B0, 0, 0); PG8_LDB(B1, 0, 1); PG8_SCHED; PG8_LDA(At, 0, 0); PG8_STAGE(PG8_SA(1, 1), a1, va[1]);
;             PG8_WAIT_V(8); PG8_WAIT_L(0); PG8_BAR; PG8_MMA(0, 0, At, B0); PG8_MMA(0, 1, At, B1); PG8_BAR; PG8_SCHED;
;             if (last && has_next) { PG8_AOFFS(va, nxt); }
;             PG8_LDA(At, 0, 1); PG8_STAGE(PG8_SB(0, 0), b2, voffB); PG8_STAGE(PG8_SB(0, 1), b2 + hstepB, voffB); PG8_STAGE(PG8_SA(0, 0), a2, va[0]);
;             PG8_WAIT_V(8); PG8_WAIT_L(0); PG8_BAR; PG8_MMA(1, 0, At, B0); PG8_MMA(1, 1, At, B1); PG8_BAR; PG8_SCHED;
;             PG8_LDB(B0, 1, 0); PG8_LDB(B1, 1, 1); PG8_SCHED; PG8_LDA(At, 1, 0); PG8_STAGE(PG8_SA(0, 1), a2, va[1]);
;             PG8_WAIT_V(8); PG8_WAIT_L(0); PG8_BAR; PG8_MMA(0, 0, At, B0); PG8_MMA(0, 1, At, B1); PG8_BAR; PG8_SCHED;
;             PG8_LDA(At, 1, 1); PG8_STAGE(PG8_SB(1, 0), b3, voffB); PG8_STAGE(PG8_SB(1, 1), b3 + hstepB, voffB); PG8_STAGE(PG8_SA(1, 0), a3, va[0]);
;             PG8_WAIT_V(8); PG8_WAIT_L(0); PG8_BAR; PG8_MMA(1, 0, At, B0); PG8_MMA(1, 1, At, B1); PG8_BAR; PG8_SCHED;
	s_add_i32 s48, 0, 0x18000
	s_add_i32 s49, 0, 0x1c000
	v_add_u32_e32 v14, s48, v219
	v_add_u32_e32 v30, s49, v219
	ds_read_b128 v[2:5], v14
	ds_read_b128 v[6:9], v14 offset:1024
	ds_read_b128 v[10:13], v14 offset:2048
	ds_read_b128 v[14:17], v14 offset:3072
	ds_read_b128 v[18:21], v30
	ds_read_b128 v[22:25], v30 offset:1024
	ds_read_b128 v[26:29], v30 offset:2048
	ds_read_b128 v[30:33], v30 offset:3072
	v_mov_b32_e32 v194, v224
	s_mov_b32 m0, s57
	ds_read_b128 v[34:37], v226 offset:32768
	ds_read_b128 v[38:41], v226 offset:33792
	ds_read_b128 v[42:45], v226 offset:34816
	ds_read_b128 v[46:49], v226 offset:35840
	ds_read_b128 v[50:53], v226 offset:36864
	ds_read_b128 v[54:57], v226 offset:37888
	ds_read_b128 v[58:61], v226 offset:38912
	ds_read_b128 v[62:65], v226 offset:39936
	s_nop 0
	global_load_lds_dwordx4 v194, s[44:45]
	v_mov_b32_e32 v194, v225
	s_mov_b32 m0, s58
	s_nop 0
	global_load_lds_dwordx4 v194, s[44:45]
	s_waitcnt vmcnt(8)
	s_waitcnt lgkmcnt(0)
	s_barrier
	s_setprio 1
	s_waitcnt lgkmcnt(0)
	v_mfma_scale_f32_16x16x128_f8f6f4 v[178:181], v[2:9], v[34:41], v[178:181], v227, v227 op_sel_hi:[0,0,0]
	v_mfma_scale_f32_16x16x128_f8f6f4 v[182:185], v[10:17], v[34:41], v[182:185], v227, v227 op_sel_hi:[0,0,0]
	v_mfma_scale_f32_16x16x128_f8f6f4 v[174:177], v[2:9], v[42:49], v[174:177], v227, v227 op_sel_hi:[0,0,0]
	v_mfma_scale_f32_16x16x128_f8f6f4 v[166:169], v[10:17], v[42:49], v[166:169], v227, v227 op_sel_hi:[0,0,0]
	v_mfma_scale_f32_16x16x128_f8f6f4 v[162:165], v[2:9], v[50:57], v[162:165], v227, v227 op_sel_hi:[0,0,0]
	v_mfma_scale_f32_16x16x128_f8f6f4 v[154:157], v[10:17], v[50:57], v[154:157], v227, v227 op_sel_hi:[0,0,0]
	v_mfma_scale_f32_16x16x128_f8f6f4 v[150:153], v[2:9], v[58:65], v[150:153], v227, v227 op_sel_hi:[0,0,0]
	v_mfma_scale_f32_16x16x128_f8f6f4 v[142:145], v[10:17], v[58:65], v[142:145], v227, v227 op_sel_hi:[0,0,0]
	s_setprio 0
	s_setprio 1
	v_mfma_scale_f32_16x16x128_f8f6f4 v[186:189], v[18:25], v[34:41], v[186:189], v227, v227 op_sel_hi:[0,0,0]
	v_mfma_scale_f32_16x16x128_f8f6f4 v[190:193], v[26:33], v[34:41], v[190:193], v227, v227 op_sel_hi:[0,0,0]
	v_mfma_scale_f32_16x16x128_f8f6f4 v[170:173], v[18:25], v[42:49], v[170:173], v227, v227 op_sel_hi:[0,0,0]
	v_mfma_scale_f32_16x16x128_f8f6f4 v[158:161], v[26:33], v[42:49], v[158:161], v227, v227 op_sel_hi:[0,0,0]
	v_mfma_scale_f32_16x16x128_f8f6f4 v[146:149], v[18:25], v[50:57], v[146:149], v227, v227 op_sel_hi:[0,0,0]
	v_mfma_scale_f32_16x16x128_f8f6f4 v[138:141], v[26:33], v[50:57], v[138:141], v227, v227 op_sel_hi:[0,0,0]
	v_mfma_scale_f32_16x16x128_f8f6f4 v[134:137], v[18:25], v[58:65], v[134:137], v227, v227 op_sel_hi:[0,0,0]
	v_mfma_scale_f32_16x16x128_f8f6f4 v[130:133], v[26:33], v[58:65], v[130:133], v227, v227 op_sel_hi:[0,0,0]
	s_setprio 0
	s_barrier
	v_mov_b32_e32 v194, v215
	ds_read_b128 v[34:37], v226 offset:49152
	ds_read_b128 v[38:41], v226 offset:50176
	ds_read_b128 v[42:45], v226 offset:51200
	ds_read_b128 v[46:49], v226 offset:52224
	ds_read_b128 v[50:53], v226 offset:53248
	ds_read_b128 v[54:57], v226 offset:54272
	ds_read_b128 v[58:61], v226 offset:55296
	ds_read_b128 v[62:65], v226 offset:56320
	s_add_i32 s48, s48, s38
	v_lshl_add_u64 v[232:233], s[46:47], 0, v[194:195]
	v_lshl_add_u64 v[232:233], v[232:233], 0, s[14:15]
	s_mov_b32 m0, s48
	v_mov_b32_e32 v194, v217
	global_load_lds_dwordx4 v[232:233], off
	s_add_i32 m0, s48, 0x2000
	s_nop 0
	v_lshl_add_u64 v[232:233], s[46:47], 0, v[194:195]
	s_add_u32 s46, s46, 0xb0080
	v_lshl_add_u64 v[232:233], v[232:233], 0, s[14:15]
	s_addc_u32 s47, s47, 0
	v_mov_b32_e32 v194, v215
	s_add_i32 s48, s49, s38
	global_load_lds_dwordx4 v[232:233], off
	s_mov_b32 m0, s48
	s_nop 0
	global_load_lds_dwordx4 v194, s[46:47]
	v_mov_b32_e32 v194, v217
	s_add_i32 m0, s48, 0x2000
	s_nop 0
	global_load_lds_dwordx4 v194, s[46:47]
	v_mov_b32_e32 v194, v222
	s_mov_b32 m0, s62
	v_lshl_add_u64 v[232:233], s[44:45], 0, v[194:195]
	v_lshl_add_u64 v[232:233], v[232:233], 0, s[14:15]
	v_mov_b32_e32 v194, v223
	global_load_lds_dwordx4 v[232:233], off
	s_mov_b32 m0, s63
	v_lshl_add_u64 v[232:233], s[44:45], 0, v[194:195]
	v_lshl_add_u64 v[232:233], v[232:233], 0, s[14:15]
	global_load_lds_dwordx4 v[232:233], off
	s_waitcnt vmcnt(8)
	s_waitcnt lgkmcnt(0)
	s_barrier
	s_setprio 1
	s_waitcnt lgkmcnt(0)
	v_mfma_scale_f32_16x16x128_f8f6f4 v[126:129], v[2:9], v[34:41], v[126:129], v227, v227 op_sel_hi:[0,0,0]
	v_mfma_scale_f32_16x16x128_f8f6f4 v[122:125], v[10:17], v[34:41], v[122:125], v227, v227 op_sel_hi:[0,0,0]
	v_mfma_scale_f32_16x16x128_f8f6f4 v[114:117], v[2:9], v[42:49], v[114:117], v227, v227 op_sel_hi:[0,0,0]
	v_mfma_scale_f32_16x16x128_f8f6f4 v[110:113], v[10:17], v[42:49], v[110:113], v227, v227 op_sel_hi:[0,0,0]
	v_mfma_scale_f32_16x16x128_f8f6f4 v[102:105], v[2:9], v[50:57], v[102:105], v227, v227 op_sel_hi:[0,0,0]
	v_mfma_scale_f32_16x16x128_f8f6f4 v[94:97], v[10:17], v[50:57], v[94:97], v227, v227 op_sel_hi:[0,0,0]
	v_mfma_scale_f32_16x16x128_f8f6f4 v[86:89], v[2:9], v[58:65], v[86:89], v227, v227 op_sel_hi:[0,0,0]
	v_mfma_scale_f32_16x16x128_f8f6f4 v[78:81], v[10:17], v[58:65], v[78:81], v227, v227 op_sel_hi:[0,0,0]
	s_setprio 0
	s_setprio 1
	v_mfma_scale_f32_16x16x128_f8f6f4 v[118:121], v[18:25], v[34:41], v[118:121], v227, v227 op_sel_hi:[0,0,0]
	v_mfma_scale_f32_16x16x128_f8f6f4 v[106:109], v[26:33], v[34:41], v[106:109], v227, v227 op_sel_hi:[0,0,0]
	v_mfma_scale_f32_16x16x128_f8f6f4 v[98:101], v[18:25], v[42:49], v[98:101], v227, v227 op_sel_hi:[0,0,0]
	v_mfma_scale_f32_16x16x128_f8f6f4 v[90:93], v[26:33], v[42:49], v[90:93], v227, v227 op_sel_hi:[0,0,0]
	v_mfma_scale_f32_16x16x128_f8f6f4 v[82:85], v[18:25], v[50:57], v[82:85], v227, v227 op_sel_hi:[0,0,0]
	v_mfma_scale_f32_16x16x128_f8f6f4 v[74:77], v[26:33], v[50:57], v[74:77], v227, v227 op_sel_hi:[0,0,0]
	v_mfma_scale_f32_16x16x128_f8f6f4 v[70:73], v[18:25], v[58:65], v[70:73], v227, v227 op_sel_hi:[0,0,0]
	v_mfma_scale_f32_16x16x128_f8f6f4 v[66:69], v[26:33], v[58:65], v[66:69], v227, v227 op_sel_hi:[0,0,0]
	s_setprio 0
	s_barrier
	s_cmp_ge_i32 s71, s35
	s_cbranch_scc1 .LBB0_1568
	s_mov_b64 s[46:47], s[42:43]
	s_branch .LBB0_1564

; #define PG8_STAGE(bufoff, gbase, voff) do { _Pragma("unroll") for (int _i = 0; _i < 2; ++_i) { unsigned vo_ = (voff)[_i]; asm volatile("" : "+v"(vo_));   \
;         __builtin_amdgcn_global_load_lds((const unsigned*)((const char*)(gbase) + vo_), (LAS unsigned*)(lds + (bufoff) + ldsw + _i * 8192), 16, 0, 0); } } while (0)
; #define PG8_LDA(dst, b, h) do { _Pragma("unroll") for (int m = 0; m < 4; ++m) _Pragma("unroll") for (int k = 0; k < 2; ++k) dst[m][k] = *(const LAS bf16x8*)(lds + PG8_SA(b, h) + aoff + m * 2048 + k * 1024); } while (0)
; #define PG8_LDB(dst, b, h) do { _Pragma("unroll") for (int n = 0; n < 2; ++n) _Pragma("unroll") for (int k = 0; k < 2; ++k) dst[n][k] = *(const LAS bf16x8*)(lds + PG8_SB(b, h) + boff + n * 2048 + k * 1024); } while (0)
; #define PG8_WAIT_V(n) asm volatile("s_waitcnt vmcnt(" #n ")" ::: "memory")
; #define PG8_WAIT_L(n) asm volatile("s_waitcnt lgkmcnt(" #n ")" ::: "memory")
; #define PG8_BAR __builtin_amdgcn_s_barrier()
; #define PG8_SCHED __builtin_amdgcn_sched_barrier(0)
; #define PG8_AOFFS(dst, un) do { _Pragma("unroll") for (int _h = 0; _h < 2; ++_h) _Pragma("unroll") for (int _i = 0; _i < 2; ++_i) dst[_h][_i] = S.Aoff(un, _h * HALF + Rr[_i]) + (unsigned)Cc[_i] * 2u; } while (0)
;     ...
;             PG8_LDB(B0, 0, 0); PG8_LDB(B1, 0, 1); PG8_SCHED; PG8_LDA(At, 0, 0); PG8_STAGE(PG8_SA(1, 1), a1, va[1]);
;             PG8_WAIT_V(8); PG8_WAIT_L(0); PG8_BAR; PG8_MMA(0, 0, At, B0); PG8_MMA(0, 1, At, B1); PG8_BAR; PG8_SCHED;
;             if (last && has_next) { PG8_AOFFS(va, nxt); }
;             PG8_LDA(At, 0, 1); PG8_STAGE(PG8_SB(0, 0), b2, voffB); PG8_STAGE(PG8_SB(0, 1), b2 + hstepB, voffB); PG8_STAGE(PG8_SA(0, 0), a2, va[0]);
;             PG8_WAIT_V(8); PG8_WAIT_L(0); PG8_BAR; PG8_MMA(1, 0, At, B0); PG8_MMA(1, 1, At, B1); PG8_BAR; PG8_SCHED;
;             PG8_LDB(B0, 1, 0); PG8_LDB(B1, 1, 1); PG8_SCHED; PG8_LDA(At, 1, 0); PG8_STAGE(PG8_SA(0, 1), a2, va[1]);
;             PG8_WAIT_V(8); PG8_WAIT_L(0); PG8_BAR; PG8_MMA(0, 0, At, B0); PG8_MMA(0, 1, At, B1); PG8_BAR; PG8_SCHED;
;             PG8_LDA(At, 1, 1); PG8_STAGE(PG8_SB(1, 0), b3, voffB); PG8_STAGE(PG8_SB(1, 1), b3 + hstepB, voffB); PG8_STAGE(PG8_SA(1, 0), a3, va[0]);
;             PG8_WAIT_V(8); PG8_WAIT_L(0); PG8_BAR; PG8_MMA(1, 0, At, B0); PG8_MMA(1, 1, At, B1); PG8_BAR; PG8_SCHED;
.LBB0_2638:
	ds_read_b128 v[18:21], v214
	ds_read_b128 v[22:25], v214 offset:1024
	ds_read_b128 v[26:29], v214 offset:2048
	ds_read_b128 v[30:33], v214 offset:3072
	ds_read_b128 v[2:5], v215
	ds_read_b128 v[6:9], v215 offset:1024
	ds_read_b128 v[10:13], v215 offset:2048
	ds_read_b128 v[14:17], v215 offset:3072
	s_cmp_eq_u32 s89, 52
	s_cselect_b64 s[6:7], -1, 0
	v_mov_b32_e32 v194, v208
	s_add_u32 s56, s24, s54
	s_mov_b32 m0, s79
	ds_read_b128 v[58:61], v216
	ds_read_b128 v[62:65], v216 offset:1024
	ds_read_b128 v[50:53], v216 offset:2048
	ds_read_b128 v[54:57], v216 offset:3072
	ds_read_b128 v[42:45], v216 offset:4096
	ds_read_b128 v[46:49], v216 offset:5120
	ds_read_b128 v[34:37], v216 offset:6144
	ds_read_b128 v[38:41], v216 offset:7168
	s_addc_u32 s57, s25, s55
	global_load_lds_dwordx4 v194, s[56:57]
	v_mov_b32_e32 v194, v209
	s_mov_b32 m0, s80
	s_nop 0
	global_load_lds_dwordx4 v194, s[56:57]
	s_waitcnt vmcnt(8)
	s_waitcnt lgkmcnt(0)
	s_barrier
	s_setprio 1
	s_waitcnt lgkmcnt(0)
	v_mfma_scale_f32_16x16x128_f8f6f4 v[242:245], v[2:9], v[58:65], v[166:169], v217, v217 op_sel_hi:[0,0,0]
	v_mfma_scale_f32_16x16x128_f8f6f4 v[190:193], v[18:25], v[58:65], v[190:193], v217, v217 op_sel_hi:[0,0,0]
	v_mfma_scale_f32_16x16x128_f8f6f4 v[186:189], v[26:33], v[58:65], v[186:189], v217, v217 op_sel_hi:[0,0,0]
	v_mfma_scale_f32_16x16x128_f8f6f4 v[246:249], v[10:17], v[58:65], v[162:165], v217, v217 op_sel_hi:[0,0,0]
	v_mfma_scale_f32_16x16x128_f8f6f4 v[182:185], v[18:25], v[50:57], v[182:185], v217, v217 op_sel_hi:[0,0,0]
	v_mfma_scale_f32_16x16x128_f8f6f4 v[178:181], v[26:33], v[50:57], v[178:181], v217, v217 op_sel_hi:[0,0,0]
	v_mfma_scale_f32_16x16x128_f8f6f4 v[150:153], v[2:9], v[50:57], v[150:153], v217, v217 op_sel_hi:[0,0,0]
	v_mfma_scale_f32_16x16x128_f8f6f4 v[146:149], v[10:17], v[50:57], v[146:149], v217, v217 op_sel_hi:[0,0,0]
	s_setprio 0
	s_setprio 1
	v_mfma_scale_f32_16x16x128_f8f6f4 v[174:177], v[18:25], v[42:49], v[174:177], v217, v217 op_sel_hi:[0,0,0]
	v_mfma_scale_f32_16x16x128_f8f6f4 v[170:173], v[26:33], v[42:49], v[170:173], v217, v217 op_sel_hi:[0,0,0]
	v_mfma_scale_f32_16x16x128_f8f6f4 v[142:145], v[2:9], v[42:49], v[142:145], v217, v217 op_sel_hi:[0,0,0]
	v_mfma_scale_f32_16x16x128_f8f6f4 v[138:141], v[10:17], v[42:49], v[138:141], v217, v217 op_sel_hi:[0,0,0]
	v_mfma_scale_f32_16x16x128_f8f6f4 v[158:161], v[18:25], v[34:41], v[158:161], v217, v217 op_sel_hi:[0,0,0]
	v_mfma_scale_f32_16x16x128_f8f6f4 v[154:157], v[26:33], v[34:41], v[154:157], v217, v217 op_sel_hi:[0,0,0]
	v_mfma_scale_f32_16x16x128_f8f6f4 v[126:129], v[2:9], v[34:41], v[126:129], v217, v217 op_sel_hi:[0,0,0]
	v_mfma_scale_f32_16x16x128_f8f6f4 v[122:125], v[10:17], v[34:41], v[122:125], v217, v217 op_sel_hi:[0,0,0]
	s_setprio 0
	s_barrier
	s_and_b64 s[56:57], s[4:5], s[6:7]
	s_andn2_b64 vcc, exec, s[56:57]
	s_cbranch_vccnz .LBB0_2640
	v_mov_b32_e32 v209, v224
	v_mov_b32_e32 v208, v223
	v_mov_b32_e32 v207, v222
	v_mov_b32_e32 v206, v221
.LBB0_2640:
	s_add_u32 s56, s54, 0x100
	s_waitcnt lgkmcnt(0)
	s_addc_u32 s57, s55, 0
	v_mov_b32_e32 v194, v203
	s_mov_b32 m0, s61
	s_and_b64 s[58:59], s[6:7], exec
	s_cselect_b32 s58, 0, s56
	v_lshl_add_u64 v[166:167], v[198:199], 0, s[54:55]
	v_cndmask_b32_e64 v201, v167, v197, s[6:7]
	v_cndmask_b32_e64 v200, v166, v196, s[6:7]
	s_cselect_b32 s59, 0, s57
	s_add_u32 s58, s14, s58
	s_addc_u32 s59, s15, s59
	v_readfirstlane_b32 s6, v200
	v_readfirstlane_b32 s7, v201
	ds_read_b128 v[58:61], v216 offset:16384
	ds_read_b128 v[62:65], v216 offset:17408
	ds_read_b128 v[162:165], v216 offset:18432
	ds_read_b128 v[166:169], v216 offset:19456
	ds_read_b128 v[226:229], v216 offset:20480
	ds_read_b128 v[230:233], v216 offset:21504
	ds_read_b128 v[234:237], v216 offset:22528
	ds_read_b128 v[238:241], v216 offset:23552
	s_nop 0
	global_load_lds_dwordx4 v194, s[6:7]
	v_mov_b32_e32 v194, v205
	s_mov_b32 m0, s62
	s_nop 0
	global_load_lds_dwordx4 v194, s[6:7]
	s_mov_b32 m0, s63
	v_lshl_add_u64 v[50:51], v[200:201], 0, s[16:17]
	v_mov_b32_e32 v52, v203
	v_readfirstlane_b32 s6, v50
	v_readfirstlane_b32 s7, v51
	v_mov_b32_e32 v50, v205
	s_nop 3
	global_load_lds_dwordx4 v52, s[6:7]
	s_mov_b32 m0, s64
	s_nop 0
	global_load_lds_dwordx4 v50, s[6:7]
	s_mov_b32 m0, s60
	v_mov_b32_e32 v42, v206
	s_nop 0
	global_load_lds_dwordx4 v42, s[58:59]
	v_mov_b32_e32 v42, v207
	s_mov_b32 m0, s65
	s_nop 0
	global_load_lds_dwordx4 v42, s[58:59]
	s_waitcnt vmcnt(8)
	s_waitcnt lgkmcnt(0)
	s_barrier
	s_setprio 1
	s_waitcnt lgkmcnt(0)
	v_mfma_scale_f32_16x16x128_f8f6f4 v[134:137], v[18:25], v[58:65], v[134:137], v217, v217 op_sel_hi:[0,0,0]
	v_mfma_scale_f32_16x16x128_f8f6f4 v[130:133], v[26:33], v[58:65], v[130:133], v217, v217 op_sel_hi:[0,0,0]
	v_mfma_scale_f32_16x16x128_f8f6f4 v[114:117], v[18:25], v[162:169], v[114:117], v217, v217 op_sel_hi:[0,0,0]
	v_mfma_scale_f32_16x16x128_f8f6f4 v[106:109], v[26:33], v[162:169], v[106:109], v217, v217 op_sel_hi:[0,0,0]
	v_mfma_scale_f32_16x16x128_f8f6f4 v[98:101], v[18:25], v[226:233], v[98:101], v217, v217 op_sel_hi:[0,0,0]
	v_mfma_scale_f32_16x16x128_f8f6f4 v[90:93], v[26:33], v[226:233], v[90:93], v217, v217 op_sel_hi:[0,0,0]
	v_mfma_scale_f32_16x16x128_f8f6f4 v[82:85], v[18:25], v[234:241], v[82:85], v217, v217 op_sel_hi:[0,0,0]
	v_mfma_scale_f32_16x16x128_f8f6f4 v[74:77], v[26:33], v[234:241], v[74:77], v217, v217 op_sel_hi:[0,0,0]
	s_setprio 0
	s_setprio 1
	v_mfma_scale_f32_16x16x128_f8f6f4 v[118:121], v[2:9], v[58:65], v[118:121], v217, v217 op_sel_hi:[0,0,0]
	v_mfma_scale_f32_16x16x128_f8f6f4 v[110:113], v[10:17], v[58:65], v[110:113], v217, v217 op_sel_hi:[0,0,0]
	v_mfma_scale_f32_16x16x128_f8f6f4 v[102:105], v[2:9], v[162:169], v[102:105], v217, v217 op_sel_hi:[0,0,0]
	v_mfma_scale_f32_16x16x128_f8f6f4 v[94:97], v[10:17], v[162:169], v[94:97], v217, v217 op_sel_hi:[0,0,0]
	v_mfma_scale_f32_16x16x128_f8f6f4 v[86:89], v[2:9], v[226:233], v[86:89], v217, v217 op_sel_hi:[0,0,0]
	v_mfma_scale_f32_16x16x128_f8f6f4 v[78:81], v[10:17], v[226:233], v[78:81], v217, v217 op_sel_hi:[0,0,0]
	v_mfma_scale_f32_16x16x128_f8f6f4 v[70:73], v[2:9], v[234:241], v[70:73], v217, v217 op_sel_hi:[0,0,0]
	v_mfma_scale_f32_16x16x128_f8f6f4 v[66:69], v[10:17], v[234:241], v[66:69], v217, v217 op_sel_hi:[0,0,0]
	s_setprio 0
	s_barrier
; #define PG8_STAGE(bufoff, gbase, voff) do { _Pragma("unroll") for (int _i = 0; _i < 2; ++_i) { unsigned vo_ = (voff)[_i]; asm volatile("" : "+v"(vo_));   \
;         __builtin_amdgcn_global_load_lds((const unsigned*)((const char*)(gbase) + vo_), (LAS unsigned*)(lds + (bufoff) + ldsw + _i * 8192), 16, 0, 0); } } while (0)
; #define PG8_LDA(dst, b, h) do { _Pragma("unroll") for (int m = 0; m < 4; ++m) _Pragma("unroll") for (int k = 0; k < 2; ++k) dst[m][k] = *(const LAS bf16x8*)(lds + PG8_SA(b, h) + aoff + m * 2048 + k * 1024); } while (0)
; #define PG8_LDB(dst, b, h) do { _Pragma("unroll") for (int n = 0; n < 2; ++n) _Pragma("unroll") for (int k = 0; k < 2; ++k) dst[n][k] = *(const LAS bf16x8*)(lds + PG8_SB(b, h) + boff + n * 2048 + k * 1024); } while (0)
; #define PG8_WAIT_V(n) asm volatile("s_waitcnt vmcnt(" #n ")" ::: "memory")
; #define PG8_WAIT_L(n) asm volatile("s_waitcnt lgkmcnt(" #n ")" ::: "memory")
; #define PG8_BAR __builtin_amdgcn_s_barrier()
; #define PG8_SCHED __builtin_amdgcn_sched_barrier(0)
; #define PG8_AOFFS(dst, un) do { _Pragma("unroll") for (int _h = 0; _h < 2; ++_h) _Pragma("unroll") for (int _i = 0; _i < 2; ++_i) dst[_h][_i] = S.Aoff(un, _h * HALF + Rr[_i]) + (unsigned)Cc[_i] * 2u; } while (0)
;     ...
;             PG8_LDB(B0, 0, 0); PG8_LDB(B1, 0, 1); PG8_SCHED; PG8_LDA(At, 0, 0); PG8_STAGE(PG8_SA(1, 1), a1, va[1]);
;             PG8_WAIT_V(8); PG8_WAIT_L(0); PG8_BAR; PG8_MMA(0, 0, At, B0); PG8_MMA(0, 1, At, B1); PG8_BAR; PG8_SCHED;
;             if (last && has_next) { PG8_AOFFS(va, nxt); }
;             PG8_LDA(At, 0, 1); PG8_STAGE(PG8_SB(0, 0), b2, voffB); PG8_STAGE(PG8_SB(0, 1), b2 + hstepB, voffB); PG8_STAGE(PG8_SA(0, 0), a2, va[0]);
;             PG8_WAIT_V(8); PG8_WAIT_L(0); PG8_BAR; PG8_MMA(1, 0, At, B0); PG8_MMA(1, 1, At, B1); PG8_BAR; PG8_SCHED;
;             PG8_LDB(B0, 1, 0); PG8_LDB(B1, 1, 1); PG8_SCHED; PG8_LDA(At, 1, 0); PG8_STAGE(PG8_SA(0, 1), a2, va[1]);
;             PG8_WAIT_V(8); PG8_WAIT_L(0); PG8_BAR; PG8_MMA(0, 0, At, B0); PG8_MMA(0, 1, At, B1); PG8_BAR; PG8_SCHED;
;             PG8_LDA(At, 1, 1); PG8_STAGE(PG8_SB(1, 0), b3, voffB); PG8_STAGE(PG8_SB(1, 1), b3 + hstepB, voffB); PG8_STAGE(PG8_SA(1, 0), a3, va[0]);
;             PG8_WAIT_V(8); PG8_WAIT_L(0); PG8_BAR; PG8_MMA(1, 0, At, B0); PG8_MMA(1, 1, At, B1); PG8_BAR; PG8_SCHED;
	s_add_i32 s6, 0, 0x18000
	s_add_i32 s7, 0, 0x1c000
	v_add_u32_e32 v14, s6, v211
	v_add_u32_e32 v30, s7, v211
	ds_read_b128 v[2:5], v14
	ds_read_b128 v[6:9], v14 offset:1024
	ds_read_b128 v[10:13], v14 offset:2048
	ds_read_b128 v[14:17], v14 offset:3072
	ds_read_b128 v[18:21], v30
	ds_read_b128 v[22:25], v30 offset:1024
	ds_read_b128 v[26:29], v30 offset:2048
	ds_read_b128 v[30:33], v30 offset:3072
	v_mov_b32_e32 v162, v208
	s_mov_b32 m0, s66
	ds_read_b128 v[34:37], v216 offset:32768
	ds_read_b128 v[38:41], v216 offset:33792
	ds_read_b128 v[42:45], v216 offset:34816
	ds_read_b128 v[46:49], v216 offset:35840
	ds_read_b128 v[50:53], v216 offset:36864
	ds_read_b128 v[54:57], v216 offset:37888
	ds_read_b128 v[58:61], v216 offset:38912
	ds_read_b128 v[62:65], v216 offset:39936
	s_nop 0
	global_load_lds_dwordx4 v162, s[58:59]
	v_mov_b32_e32 v162, v209
	s_mov_b32 m0, s67
	s_nop 0
	global_load_lds_dwordx4 v162, s[58:59]
	s_waitcnt vmcnt(8)
	s_waitcnt lgkmcnt(0)
	s_barrier
	s_setprio 1
	s_waitcnt lgkmcnt(0)
	v_mfma_scale_f32_16x16x128_f8f6f4 v[190:193], v[2:9], v[34:41], v[190:193], v217, v217 op_sel_hi:[0,0,0]
	v_mfma_scale_f32_16x16x128_f8f6f4 v[186:189], v[10:17], v[34:41], v[186:189], v217, v217 op_sel_hi:[0,0,0]
	v_mfma_scale_f32_16x16x128_f8f6f4 v[182:185], v[2:9], v[42:49], v[182:185], v217, v217 op_sel_hi:[0,0,0]
	v_mfma_scale_f32_16x16x128_f8f6f4 v[178:181], v[10:17], v[42:49], v[178:181], v217, v217 op_sel_hi:[0,0,0]
	v_mfma_scale_f32_16x16x128_f8f6f4 v[174:177], v[2:9], v[50:57], v[174:177], v217, v217 op_sel_hi:[0,0,0]
	v_mfma_scale_f32_16x16x128_f8f6f4 v[170:173], v[10:17], v[50:57], v[170:173], v217, v217 op_sel_hi:[0,0,0]
	v_mfma_scale_f32_16x16x128_f8f6f4 v[158:161], v[2:9], v[58:65], v[158:161], v217, v217 op_sel_hi:[0,0,0]
	v_mfma_scale_f32_16x16x128_f8f6f4 v[154:157], v[10:17], v[58:65], v[154:157], v217, v217 op_sel_hi:[0,0,0]
	s_setprio 0
	s_setprio 1
	v_mfma_scale_f32_16x16x128_f8f6f4 v[166:169], v[18:25], v[34:41], v[242:245], v217, v217 op_sel_hi:[0,0,0]
	v_mfma_scale_f32_16x16x128_f8f6f4 v[162:165], v[26:33], v[34:41], v[246:249], v217, v217 op_sel_hi:[0,0,0]
	v_mfma_scale_f32_16x16x128_f8f6f4 v[150:153], v[18:25], v[42:49], v[150:153], v217, v217 op_sel_hi:[0,0,0]
	v_mfma_scale_f32_16x16x128_f8f6f4 v[146:149], v[26:33], v[42:49], v[146:149], v217, v217 op_sel_hi:[0,0,0]
	v_mfma_scale_f32_16x16x128_f8f6f4 v[142:145], v[18:25], v[50:57], v[142:145], v217, v217 op_sel_hi:[0,0,0]
	v_mfma_scale_f32_16x16x128_f8f6f4 v[138:141], v[26:33], v[50:57], v[138:141], v217, v217 op_sel_hi:[0,0,0]
	v_mfma_scale_f32_16x16x128_f8f6f4 v[126:129], v[18:25], v[58:65], v[126:129], v217, v217 op_sel_hi:[0,0,0]
	v_mfma_scale_f32_16x16x128_f8f6f4 v[122:125], v[26:33], v[58:65], v[122:125], v217, v217 op_sel_hi:[0,0,0]
	s_setprio 0
	s_barrier
	v_mov_b32_e32 v194, v203
	ds_read_b128 v[34:37], v216 offset:49152
	ds_read_b128 v[38:41], v216 offset:50176
	ds_read_b128 v[42:45], v216 offset:51200
	ds_read_b128 v[46:49], v216 offset:52224
	ds_read_b128 v[50:53], v216 offset:53248
	ds_read_b128 v[54:57], v216 offset:54272
	ds_read_b128 v[58:61], v216 offset:55296
	ds_read_b128 v[62:65], v216 offset:56320
	s_add_i32 s6, s6, s35
	v_lshl_add_u64 v[226:227], v[200:201], 0, v[194:195]
	v_lshl_add_u64 v[226:227], v[226:227], 0, s[22:23]
	s_mov_b32 m0, s6
	v_mov_b32_e32 v194, v205
	global_load_lds_dwordx4 v[226:227], off
	s_add_i32 m0, s6, 0x2000
	v_lshl_add_u64 v[226:227], v[200:201], 0, v[194:195]
	v_lshl_add_u64 v[226:227], v[226:227], 0, s[22:23]
	v_lshl_add_u64 v[200:201], v[200:201], 0, s[26:27]
	v_mov_b32_e32 v194, v203
	s_add_i32 s54, s7, s35
	global_load_lds_dwordx4 v[226:227], off
	v_readfirstlane_b32 s6, v200
	v_readfirstlane_b32 s7, v201
	s_mov_b32 m0, s54
	s_nop 3
	global_load_lds_dwordx4 v194, s[6:7]
	v_mov_b32_e32 v194, v205
	s_add_i32 m0, s54, 0x2000
	s_nop 0
	global_load_lds_dwordx4 v194, s[6:7]
	v_mov_b32_e32 v194, v206
	s_mov_b32 m0, s70
	v_lshl_add_u64 v[200:201], s[58:59], 0, v[194:195]
	v_lshl_add_u64 v[200:201], v[200:201], 0, s[22:23]
	v_mov_b32_e32 v194, v207
	global_load_lds_dwordx4 v[200:201], off
	s_mov_b32 m0, s71
	v_lshl_add_u64 v[200:201], s[58:59], 0, v[194:195]
	v_lshl_add_u64 v[200:201], v[200:201], 0, s[22:23]
	global_load_lds_dwordx4 v[200:201], off
	s_waitcnt vmcnt(8)
	s_waitcnt lgkmcnt(0)
	s_barrier
	s_setprio 1
	s_waitcnt lgkmcnt(0)
	v_mfma_scale_f32_16x16x128_f8f6f4 v[134:137], v[2:9], v[34:41], v[134:137], v217, v217 op_sel_hi:[0,0,0]
	v_mfma_scale_f32_16x16x128_f8f6f4 v[130:133], v[10:17], v[34:41], v[130:133], v217, v217 op_sel_hi:[0,0,0]
	v_mfma_scale_f32_16x16x128_f8f6f4 v[114:117], v[2:9], v[42:49], v[114:117], v217, v217 op_sel_hi:[0,0,0]
	v_mfma_scale_f32_16x16x128_f8f6f4 v[106:109], v[10:17], v[42:49], v[106:109], v217, v217 op_sel_hi:[0,0,0]
	v_mfma_scale_f32_16x16x128_f8f6f4 v[98:101], v[2:9], v[50:57], v[98:101], v217, v217 op_sel_hi:[0,0,0]
	v_mfma_scale_f32_16x16x128_f8f6f4 v[90:93], v[10:17], v[50:57], v[90:93], v217, v217 op_sel_hi:[0,0,0]
	v_mfma_scale_f32_16x16x128_f8f6f4 v[82:85], v[2:9], v[58:65], v[82:85], v217, v217 op_sel_hi:[0,0,0]
	v_mfma_scale_f32_16x16x128_f8f6f4 v[74:77], v[10:17], v[58:65], v[74:77], v217, v217 op_sel_hi:[0,0,0]
	s_setprio 0
	s_setprio 1
	v_mfma_scale_f32_16x16x128_f8f6f4 v[118:121], v[18:25], v[34:41], v[118:121], v217, v217 op_sel_hi:[0,0,0]
	v_mfma_scale_f32_16x16x128_f8f6f4 v[110:113], v[26:33], v[34:41], v[110:113], v217, v217 op_sel_hi:[0,0,0]
	v_mfma_scale_f32_16x16x128_f8f6f4 v[102:105], v[18:25], v[42:49], v[102:105], v217, v217 op_sel_hi:[0,0,0]
	v_mfma_scale_f32_16x16x128_f8f6f4 v[94:97], v[26:33], v[42:49], v[94:97], v217, v217 op_sel_hi:[0,0,0]
	v_mfma_scale_f32_16x16x128_f8f6f4 v[86:89], v[18:25], v[50:57], v[86:89], v217, v217 op_sel_hi:[0,0,0]
	v_mfma_scale_f32_16x16x128_f8f6f4 v[78:81], v[26:33], v[50:57], v[78:81], v217, v217 op_sel_hi:[0,0,0]
	v_mfma_scale_f32_16x16x128_f8f6f4 v[70:73], v[18:25], v[58:65], v[70:73], v217, v217 op_sel_hi:[0,0,0]
	v_mfma_scale_f32_16x16x128_f8f6f4 v[66:69], v[26:33], v[58:65], v[66:69], v217, v217 op_sel_hi:[0,0,0]
	s_setprio 0
	s_barrier
	s_add_i32 s89, s89, 2
	s_cmp_gt_u32 s89, 53
	s_cbranch_scc1 .LBB0_2642
	s_mov_b64 s[54:55], s[56:57]
	s_branch .LBB0_2638
